# v16: attention score accumulators start from a persistent -max register block (MFMA C operand) instead of 16 v_mov per tile
# speedup vs baseline: 1.0062x; 1.0062x over previous
; #define SBAR() __builtin_amdgcn_sched_barrier(0)
; #define SLOAD(k0) do { sv0 = *reinterpret_cast<const u32x4*>(Vh + (size_t)(k0) + vgo); \
;     const unsigned char* kp_ = Kh + (size_t)(k0) * LDKK; sk0 = *reinterpret_cast<const u32x4*>(kp_ + kgo0); sk1 = *reinterpret_cast<const u32x4*>(kp_ + kgo1); } while (0)
; #define SWRITE(b) do { *(u32x4*)(V_lds + (b) * SHM_V + vlo) = sv0; \
;     *(u32x4*)(K_lds + (b) * SHM_K + klo0) = sk0; *(u32x4*)(K_lds + (b) * SHM_K + klo1) = sk1; } while (0)
; #define SWAIT() asm volatile("s_waitcnt vmcnt(0)" ::: "memory")
; __device__ __forceinline__ void attn_body(const unsigned char* __restrict__ Qb, const unsigned char* __restrict__ Kh, const unsigned char* __restrict__ Vh, bf16_t* __restrict__ Ob, int seq, char* lds) {
;     ...
;     const unsigned char* Qw = Qb + (size_t)(wid * QBLK + r32) * LDQ + hi * 32;
; #pragma unroll
;     for (int s3 = 0; s3 < 3; ++s3) { const u32x4 x0 = *reinterpret_cast<const u32x4*>(Qw + s3 * 64), x1 = *reinterpret_cast<const u32x4*>(Qw + s3 * 64 + 16);
;         qf[s3] = (pg8::i32x8){(int)x0.x, (int)x0.y, (int)x0.z, (int)x0.w, (int)x1.x, (int)x1.y, (int)x1.z, (int)x1.w}; }
;     const int vd = tid >> 2, vc = tid & 3; const unsigned vgo = (unsigned)(vd * 4352 + vc * 16); const int vlo = vd * VROW + vc * 16;
;     const int id1 = tid < 256 ? tid + 512 : tid;
;     const int kr0 = tid / 12, kc0 = tid % 12, kr1 = id1 / 12, kc1 = id1 % 12;
;     const unsigned kgo0 = (unsigned)(kr0 * LDKK + kc0 * 16), kgo1 = (unsigned)(kr1 * LDKK + kc1 * 16); const int klo0 = kr0 * KROW + kc0 * 16, klo1 = kr1 * KROW + kc1 * 16;
;     const int vb0 = (int)(uintptr_t)V_lds + r32 * VROW + hi * 32;
;     const int kb = (int)(uintptr_t)K_lds + r32 * KROW + hi * 32;
;     u32x4 sv0, sk0, sk1;
;     ...
;     f32x16 pA0, pA1, pB0, pB1; float mnA, mnB, alA, alB; pg8::i32x8 pa; const int NT = seq / KVBLK;
;     const int klast = (NT - 1) * KVBLK;
;     SLOAD(0); SWAIT(); SWRITE(0); SLOAD(KVBLK); __syncthreads();
;     SWAIT(); SWRITE(1); SLOAD(2 * KVBLK); SBAR();
;     qkt(pA0, pA1, kb, qf, zf); partialSM(pA0, pA1, m_reg, mnA, alA);
.LBB0_2157:
	s_ashr_i32 s2, s44, 7
	s_lshl_b32 s6, s44, 8
	s_lshl_b32 s3, s2, 12
	s_and_b32 s6, s6, 0xf00
	s_or_b32 s12, s3, s6
	s_bfe_u32 s45, s44, 0x30004
	s_ashr_i32 s13, s12, 31
	s_mul_i32 s14, s12, 0x600
	s_mul_hi_i32 s3, s12, 0x600
	s_add_u32 s14, s9, s14
	s_mul_i32 s6, s45, 0xc0
	s_addc_u32 s3, s20, s3
	v_mov_b32_e32 v60, v0
	s_barrier
	s_add_u32 s16, s14, s6
	s_addc_u32 s17, s3, 0
	v_ashrrev_i32_e32 v3, 2, v60
	v_lshlrev_b32_e32 v5, 4, v60
	s_mul_i32 s19, s2, 0x660000
	v_mul_lo_u32 v4, v3, s34
	v_and_b32_e32 v16, 48, v5
	s_mul_hi_i32 s18, s2, 0x660000
	s_add_u32 s3, s21, s19
	v_or_b32_e32 v50, v4, v16
	v_add_u32_e32 v4, 0x200, v60
	v_cmp_gt_i32_e32 vcc, s38, v60
	v_mul_hi_i32 v5, v60, s40
	s_addc_u32 s15, s22, s18
	v_cndmask_b32_e32 v4, v60, v4, vcc
	v_lshrrev_b32_e32 v6, 31, v5
	v_ashrrev_i32_e32 v5, 1, v5
	s_add_u32 s14, s3, s6
	v_add_u32_e32 v18, v5, v6
	v_mul_hi_i32 v6, v4, s40
	s_addc_u32 s15, s15, 0
	s_lshl_b32 s2, s2, 3
	v_lshrrev_b32_e32 v7, 31, v6
	v_ashrrev_i32_e32 v6, 1, v6
	s_or_b32 s48, s2, s45
	v_add_u32_e32 v19, v6, v7
	s_mul_hi_i32 s47, s48, 0x88000
	s_mul_i32 s48, s48, 0x88000
	v_mul_lo_u32 v5, v18, 12
	v_mul_lo_u32 v6, v19, 12
	s_add_u32 s2, s23, s48
	v_sub_u32_e32 v5, v60, v5
	v_sub_u32_e32 v4, v4, v6
	v_mul_lo_u32 v6, v18, s29
	s_addc_u32 s3, s24, s47
	v_mov_b32_e32 v2, v163
	v_lshl_add_u32 v30, v5, 4, v6
	v_mul_lo_u32 v5, v19, s29
	v_lshl_add_u32 v166, v4, 4, v5
	global_load_dwordx4 v[4:7], v50, s[2:3]
	global_load_dwordx4 v[8:11], v30, s[14:15]
	global_load_dwordx4 v[12:15], v166, s[14:15]
	v_ashrrev_i32_e32 v31, 1, v60
	v_mul_lo_u32 v3, v3, s35
	v_bfi_b32 v20, s31, v31, v60
	v_add3_u32 v184, v3, v16, 0
	v_mov_b64_e32 v[16:17], s[16:17]
	s_cmp_lg_u32 0, -1
	v_and_b32_e32 v162, 32, v60
	v_mad_u64_u32 v[168:169], s[16:17], v18, s41, v[30:31]
	v_mad_i64_i32 v[16:17], s[16:17], v20, s29, v[16:17]
	v_mad_u64_u32 v[170:171], s[16:17], v19, s41, v[166:167]
	s_cselect_b32 s49, 0, 0
	s_cmp_lg_u32 s42, -1
	v_lshl_add_u64 v[16:17], v[16:17], 0, v[162:163]
	s_cselect_b32 s50, s42, 0
	s_add_u32 s16, s14, 0x18000
	global_load_dwordx4 v[134:137], v[16:17], off offset:16
	global_load_dwordx4 v[130:133], v[16:17], off
	global_load_dwordx4 v[126:129], v[16:17], off offset:80
	global_load_dwordx4 v[122:125], v[16:17], off offset:64
	global_load_dwordx4 v[118:121], v[16:17], off offset:144
	global_load_dwordx4 v[114:117], v[16:17], off offset:128
	s_waitcnt vmcnt(0)
	s_addc_u32 s17, s15, 0
	global_load_dwordx4 v[18:21], v30, s[16:17]
	global_load_dwordx4 v[22:25], v50, s[2:3] offset:64
	global_load_dwordx4 v[26:29], v166, s[16:17]
	s_add_u32 s16, s14, 0x30000
	v_add_u32_e32 v32, 0, v168
	v_add_u32_e32 v33, 0, v170
	s_addc_u32 s17, s15, 0
	v_and_b32_e32 v61, 31, v60
	v_and_b32_e32 v164, 0xffffffe0, v31
	v_mul_u32_u24_e32 v31, 0x50, v61
	v_and_b32_e32 v3, 0x3fffffc0, v60
	v_add3_u32 v171, v162, s49, v31
	v_mul_u32_u24_e32 v31, 0xd0, v61
	v_mov_b32_e32 v51, v163
	v_lshl_add_u32 v169, v3, 2, s30
	v_mov_b32_e32 v3, v2
	v_mov_b32_e32 v16, v2
	v_mov_b32_e32 v17, v2
	v_and_b32_e32 v165, 63, v60
	s_waitcnt vmcnt(11)
	ds_write_b128 v184, v[4:7]
	s_waitcnt vmcnt(10)
	ds_write_b128 v32, v[8:11] offset:30720
	s_waitcnt vmcnt(9)
	ds_write_b128 v33, v[12:15] offset:30720
	s_waitcnt lgkmcnt(0)
	s_barrier
	s_waitcnt vmcnt(0)
	global_load_dwordx4 v[138:141], v30, s[16:17]
	global_load_dwordx4 v[146:149], v50, s[2:3] offset:128
	global_load_dwordx4 v[142:145], v166, s[16:17]
	v_mov_b32_e32 v4, v2
	v_mov_b32_e32 v5, v2
	v_mov_b32_e32 v6, v2
	v_mov_b32_e32 v7, v2
	v_mov_b32_e32 v8, v2
	v_mov_b32_e32 v9, v2
	v_mov_b32_e32 v10, v2
	v_mov_b32_e32 v11, v2
	v_mov_b32_e32 v12, v2
	v_mov_b32_e32 v13, v2
	v_mov_b32_e32 v14, v2
	v_mov_b32_e32 v15, v2
	s_mov_b32 s46, -1
	v_add3_u32 v183, v162, s50, v31
	v_lshl_add_u64 v[172:173], s[2:3], 0, v[50:51]
	v_mov_b32_e32 v162, v30
	v_mov_b32_e32 v167, v163
	s_waitcnt vmcnt(4)
	ds_write_b128 v184, v[22:25] offset:10240
	ds_write_b128 v32, v[18:21] offset:44032
	s_waitcnt vmcnt(3)
	ds_write_b128 v33, v[26:29] offset:44032
	ds_read_b128 v[52:55], v183
	ds_read_b128 v[56:59], v183 offset:16
	v_xor_b32_e32 v18, 0x80000000, v2
	v_mov_b32_e32 v19, v18
	v_mov_b32_e32 v20, v18
	v_mov_b32_e32 v21, v18
	v_mov_b32_e32 v22, v18
	v_mov_b32_e32 v23, v18
	v_mov_b32_e32 v24, v18
	v_mov_b32_e32 v25, v18
	v_mov_b32_e32 v26, v18
	v_mov_b32_e32 v27, v18
	v_mov_b32_e32 v28, v18
	v_mov_b32_e32 v29, v18
	v_mov_b32_e32 v30, v18
	v_mov_b32_e32 v31, v18
	v_mov_b32_e32 v32, v18
	v_mov_b32_e32 v33, v18
	v_lshl_add_u32 v180, v61, 2, v169
	v_cmp_gt_u32_e64 s[2:3], 32, v165
	s_waitcnt lgkmcnt(0)
	v_mfma_f32_32x32x64_f8f6f4 v[34:49], v[52:59], v[130:137], v[18:33]
	ds_read_b128 v[52:55], v183 offset:6656
	ds_read_b128 v[56:59], v183 offset:6672
	v_mov_b32_e32 v181, v163
	s_waitcnt lgkmcnt(0)
	v_mfma_f32_32x32x64_f8f6f4 v[18:33], v[52:59], v[130:137], v[18:33]
	ds_read_b128 v[52:55], v183 offset:64
	ds_read_b128 v[56:59], v183 offset:80
	s_waitcnt lgkmcnt(0)
	v_mfma_f32_32x32x64_f8f6f4 v[34:49], v[52:59], v[122:129], v[34:49]
	ds_read_b128 v[52:55], v183 offset:6720
	ds_read_b128 v[56:59], v183 offset:6736
	s_waitcnt lgkmcnt(0)
	v_mfma_f32_32x32x64_f8f6f4 v[18:33], v[52:59], v[122:129], v[18:33]
	ds_read_b128 v[52:55], v183 offset:128
	ds_read_b128 v[56:59], v183 offset:144
	s_waitcnt lgkmcnt(0)
	v_mfma_f32_32x32x64_f8f6f4 v[34:49], v[52:59], v[114:121], v[34:49]
	ds_read_b128 v[52:55], v183 offset:6784
	ds_read_b128 v[56:59], v183 offset:6800
	s_waitcnt lgkmcnt(0)
	s_barrier
; __device__ __forceinline__ void partialSM(f32x16& p0, f32x16& p1, float& m_reg, float& mn, float& alpha) {
;     float pmax;
;     { float ma = fmaxf(p0[0], p0[1]), mb = fmaxf(p0[8], p0[9]), mc = fmaxf(p1[0], p1[1]), md = fmaxf(p1[8], p1[9]);
; #pragma unroll
;       for (int r = 2; r < 8; r += 2) { ma = fmaxf(fmaxf(ma, p0[r]), p0[r + 1]); mb = fmaxf(fmaxf(mb, p0[8 + r]), p0[9 + r]); mc = fmaxf(fmaxf(mc, p1[r]), p1[r + 1]); md = fmaxf(fmaxf(md, p1[8 + r]), p1[9 + r]); }
;       pmax = fmaxf(fmaxf(ma, mb), fmaxf(mc, md)); }
;     { auto rr = __builtin_amdgcn_permlane32_swap(__float_as_uint(pmax), __float_as_uint(pmax), false, false);
;       pmax = fmaxf(__uint_as_float(rr[0]), __uint_as_float(rr[1])); }
;     if (__builtin_expect(__all(pmax - m_reg <= THR), 1)) { mn = m_reg; alpha = 1.f; }
;     else { mn = fmaxf(m_reg, pmax); alpha = __builtin_amdgcn_exp2f(m_reg - mn); m_reg = mn; }
; #pragma unroll
;     for (int r = 0; r < 16; ++r) p0[r] = p0[r] - mn;
; #pragma unroll
;     for (int r = 0; r < 16; ++r) p1[r] = p1[r] - mn;
; #pragma unroll
;     for (int r = 0; r < 16; ++r) p0[r] = __builtin_amdgcn_exp2f(p0[r]);
; __device__ __forceinline__ void qkt(f32x16& p0, f32x16& p1, const int kb, const pg8::i32x8 (&qf)[3], float minit) {
; #pragma unroll
;     for (int r = 0; r < 16; ++r) { p0[r] = -minit; p1[r] = -minit; }
; __device__ __forceinline__ void attn_body(const unsigned char* __restrict__ Qb, const unsigned char* __restrict__ Kh, const unsigned char* __restrict__ Vh, bf16_t* __restrict__ Ob, int seq, char* lds) {
;     ...
;     qkt(pA0, pA1, kb, qf, zf); partialSM(pA0, pA1, m_reg, mnA, alA);
	s_nop 15
	v_max_f32_e32 v62, v35, v35
	v_mfma_f32_32x32x64_f8f6f4 v[18:33], v[52:59], v[114:121], v[18:33]
	v_max_f32_e32 v63, v34, v34
	v_max_f32_e32 v62, v63, v62
	v_max_f32_e32 v63, v43, v43
	v_max_f32_e32 v64, v42, v42
	v_max_f32_e32 v63, v64, v63
	v_max3_f32 v54, v63, v44, v45
	v_max3_f32 v54, v54, v46, v47
	v_max3_f32 v54, v54, v48, v49
	s_nop 11
	v_max_f32_e32 v52, v27, v27
	v_max_f32_e32 v53, v26, v26
	v_max_f32_e32 v52, v53, v52
	v_max3_f32 v55, v18, v19, v20
	v_max3_f32 v52, v52, v28, v29
	v_max3_f32 v53, v62, v36, v37
	v_max3_f32 v55, v55, v21, v22
	v_max3_f32 v52, v52, v30, v31
	v_max3_f32 v53, v53, v38, v39
	v_max3_f32 v55, v55, v23, v24
	v_max3_f32 v52, v52, v32, v33
	v_max3_f32 v53, v53, v40, v41
	v_max3_f32 v52, v55, v25, v52
	v_max3_f32 v52, v53, v54, v52
	v_mov_b32_e32 v53, v52
	s_nop 1
	v_permlane32_swap_b32_e32 v52, v53
	v_max_f32_e32 v53, v53, v53
	v_max_f32_e32 v52, v52, v52
	v_max_f32_e32 v52, v52, v53
	v_add_f32_e32 v53, 0x7149f2ca, v52
	v_cmp_ge_f32_e32 vcc, s43, v53
	v_max_f32_e32 v52, 0xf149f2ca, v52
	s_cmp_eq_u64 vcc, exec
	v_sub_f32_e32 v53, 0xf149f2ca, v52
	s_cselect_b64 vcc, -1, 0
	v_exp_f32_e32 v53, v53
	v_cndmask_b32_e32 v185, v52, v1, vcc
	v_sub_f32_e32 v34, v34, v185
	v_sub_f32_e32 v35, v35, v185
	v_sub_f32_e32 v36, v36, v185
	v_sub_f32_e32 v37, v37, v185
	v_sub_f32_e32 v38, v38, v185
	v_sub_f32_e32 v39, v39, v185
	v_sub_f32_e32 v40, v40, v185
	v_sub_f32_e32 v41, v41, v185
	v_sub_f32_e32 v42, v42, v185
	v_sub_f32_e32 v43, v43, v185
	v_sub_f32_e32 v44, v44, v185
	v_sub_f32_e32 v45, v45, v185
	v_sub_f32_e32 v46, v46, v185
	v_sub_f32_e32 v47, v47, v185
	v_sub_f32_e32 v48, v48, v185
	v_sub_f32_e32 v49, v49, v185
	s_add_u32 s16, s36, s48
	v_exp_f32_e32 v198, v34
	v_exp_f32_e32 v202, v35
	v_exp_f32_e32 v190, v36
	v_exp_f32_e32 v191, v37
	v_exp_f32_e32 v199, v38
	v_exp_f32_e32 v203, v39
	v_exp_f32_e32 v192, v40
	v_exp_f32_e32 v193, v41
	v_exp_f32_e32 v200, v42
	v_exp_f32_e32 v204, v43
	v_exp_f32_e32 v194, v44
	v_exp_f32_e32 v195, v45
	v_exp_f32_e32 v201, v46
	v_exp_f32_e32 v205, v47
	v_exp_f32_e32 v196, v48
	v_exp_f32_e32 v197, v49
	s_addc_u32 s17, s37, s47
	s_or_b32 s6, s19, s6
	v_sub_f32_e32 v66, v18, v185
	v_lshrrev_b32_e32 v18, 1, v60
	v_lshl_add_u64 v[174:175], s[16:17], 0, v[50:51]
	s_add_u32 s16, s27, s6
	v_cndmask_b32_e64 v186, v53, 1.0, vcc
	v_sub_f32_e32 v81, v33, v185
	v_sub_f32_e32 v80, v32, v185
	v_sub_f32_e32 v79, v31, v185
	v_sub_f32_e32 v78, v30, v185
	v_sub_f32_e32 v77, v29, v185
	v_sub_f32_e32 v76, v28, v185
	v_sub_f32_e32 v75, v27, v185
	v_sub_f32_e32 v74, v26, v185
	v_sub_f32_e32 v73, v25, v185
	v_sub_f32_e32 v72, v24, v185
	v_sub_f32_e32 v71, v23, v185
	v_sub_f32_e32 v70, v22, v185
	v_sub_f32_e32 v69, v21, v185
	v_sub_f32_e32 v68, v20, v185
	v_sub_f32_e32 v67, v19, v185
	v_and_b32_e32 v182, 16, v18
	s_addc_u32 s17, s28, s18
	v_mov_b64_e32 v[64:65], v[16:17]
	v_mov_b64_e32 v[48:49], v[16:17]
	v_mov_b64_e32 v[32:33], v[16:17]
	v_lshl_add_u64 v[176:177], s[16:17], 0, v[162:163]
	v_lshl_add_u64 v[178:179], s[16:17], 0, v[166:167]
	s_mov_b64 s[16:17], 0x396c00c0
	v_mov_b64_e32 v[62:63], v[14:15]
	v_mov_b64_e32 v[60:61], v[12:13]
	v_mov_b64_e32 v[58:59], v[10:11]
	v_mov_b64_e32 v[56:57], v[8:9]
	v_mov_b64_e32 v[54:55], v[6:7]
	v_mov_b64_e32 v[52:53], v[4:5]
	v_mov_b64_e32 v[50:51], v[2:3]
	v_mov_b64_e32 v[46:47], v[14:15]
	v_mov_b64_e32 v[44:45], v[12:13]
	v_mov_b64_e32 v[42:43], v[10:11]
	v_mov_b64_e32 v[40:41], v[8:9]
	v_mov_b64_e32 v[38:39], v[6:7]
	v_mov_b64_e32 v[36:37], v[4:5]
	v_mov_b64_e32 v[34:35], v[2:3]
	v_mov_b64_e32 v[30:31], v[14:15]
	v_mov_b64_e32 v[28:29], v[12:13]
	v_mov_b64_e32 v[26:27], v[10:11]
	v_mov_b64_e32 v[24:25], v[8:9]
	v_mov_b64_e32 v[22:23], v[6:7]
	v_mov_b64_e32 v[20:21], v[4:5]
	v_mov_b64_e32 v[18:19], v[2:3]
	s_mov_b32 s6, s7
	s_mov_b32 s47, 1
	s_mov_b32 s48, 2
	v_xor_b32_e32 v238, 0x80000000, v185
	v_mov_b32_e32 v239, v238
	v_mov_b32_e32 v240, v238
	v_mov_b32_e32 v241, v238
	v_mov_b32_e32 v242, v238
	v_mov_b32_e32 v243, v238
	v_mov_b32_e32 v244, v238
	v_mov_b32_e32 v245, v238
	v_mov_b32_e32 v246, v238
	v_mov_b32_e32 v247, v238
	v_mov_b32_e32 v248, v238
	v_mov_b32_e32 v249, v238
	v_mov_b32_e32 v250, v238
	v_mov_b32_e32 v251, v238
	v_mov_b32_e32 v252, v238
	v_mov_b32_e32 v253, v238
; #define LAS __attribute__((address_space(3)))
; #define SBAR() __builtin_amdgcn_sched_barrier(0)
; #define SLOAD(k0) do { sv0 = *reinterpret_cast<const u32x4*>(Vh + (size_t)(k0) + vgo); \
;     const unsigned char* kp_ = Kh + (size_t)(k0) * LDKK; sk0 = *reinterpret_cast<const u32x4*>(kp_ + kgo0); sk1 = *reinterpret_cast<const u32x4*>(kp_ + kgo1); } while (0)
; #define SWRITE(b) do { *(u32x4*)(V_lds + (b) * SHM_V + vlo) = sv0; \
;     *(u32x4*)(K_lds + (b) * SHM_K + klo0) = sk0; *(u32x4*)(K_lds + (b) * SHM_K + klo1) = sk1; } while (0)
; #define SWAIT() asm volatile("s_waitcnt vmcnt(0)" ::: "memory")
; __device__ __forceinline__ void qkt(f32x16& p0, f32x16& p1, const int kb, const pg8::i32x8 (&qf)[3], float minit) {
; #pragma unroll
;     for (int r = 0; r < 16; ++r) { p0[r] = -minit; p1[r] = -minit; }
; #pragma unroll
;     for (int s = 0; s < 3; ++s) {
;         const u32x4 a0 = *reinterpret_cast<const LAS u32x4*>((uintptr_t)(unsigned)(kb + (s * 64))), a1 = *reinterpret_cast<const LAS u32x4*>((uintptr_t)(unsigned)(kb + (s * 64 + 16)));
;         const u32x4 b0 = *reinterpret_cast<const LAS u32x4*>((uintptr_t)(unsigned)(kb + (s * 64 + 32 * KROW))), b1 = *reinterpret_cast<const LAS u32x4*>((uintptr_t)(unsigned)(kb + (s * 64 + 32 * KROW + 16)));
;         const pg8::i32x8 A0 = {(int)a0.x, (int)a0.y, (int)a0.z, (int)a0.w, (int)a1.x, (int)a1.y, (int)a1.z, (int)a1.w}, A1 = {(int)b0.x, (int)b0.y, (int)b0.z, (int)b0.w, (int)b1.x, (int)b1.y, (int)b1.z, (int)b1.w};
;         p0 = __builtin_amdgcn_mfma_scale_f32_32x32x64_f8f6f4(A0, qf[s], p0, 0, 0, 0, 0, 0, 0);
;         p1 = __builtin_amdgcn_mfma_scale_f32_32x32x64_f8f6f4(A1, qf[s], p1, 0, 0, 0, 0, 0, 0);
;     }
; }
; __device__ __forceinline__ void attn_body(const unsigned char* __restrict__ Qb, const unsigned char* __restrict__ Kh, const unsigned char* __restrict__ Vh, bf16_t* __restrict__ Ob, int seq, char* lds) {
;     ...
;         SWAIT(); SWRITE(bn); SLOAD(min((j + 2) * KVBLK, klast)); SBAR();
;         qkt(pB0, pB1, kb + bc * SHM_K, qf, m_reg);
;         finishSM(pA0, pA1, alA, l_reg, pa); SBAR();
;         pv_d0(o, vb0 + bm * SHM_V, pa); partialSM_shift(pB0, pB1, m_reg, alB);
;         RESC(alB); __syncthreads();
.LBB0_2158:
	s_waitcnt vmcnt(0)
	v_lshl_add_u64 v[82:83], v[174:175], 0, s[16:17]
	global_load_dwordx4 v[158:161], v[82:83], off
	global_load_dwordx4 v[154:157], v[176:177], off
	global_load_dwordx4 v[150:153], v[178:179], off
	s_mov_b32 s49, s47
	s_mov_b32 s47, s6
	s_mul_i32 s6, s48, 0x2800
	s_mul_i32 s50, s48, 0x3400
	v_add_u32_e32 v82, s6, v184
	s_add_i32 s6, s50, 0
	s_waitcnt vmcnt(4)
	ds_write_b128 v82, v[146:149]
	v_add_u32_e32 v82, s6, v168
	ds_write_b128 v82, v[138:141] offset:30720
	v_add_u32_e32 v82, s6, v170
	s_waitcnt vmcnt(3)
	ds_write_b128 v82, v[142:145] offset:30720
	s_mul_i32 s6, s49, 0x3400
	v_add_u32_e32 v146, s6, v183
	ds_read_b128 v[138:141], v146
	ds_read_b128 v[142:145], v146 offset:16
	v_exp_f32_e32 v66, v66
	v_exp_f32_e32 v67, v67
	s_waitcnt lgkmcnt(0)
	v_mfma_f32_32x32x64_f8f6f4 v[98:113], v[138:145], v[130:137], v[238:253]
	ds_read_b128 v[138:141], v146 offset:6656
	ds_read_b128 v[142:145], v146 offset:6672
	ds_read_b128 v[206:209], v146 offset:64
	ds_read_b128 v[210:213], v146 offset:80
	ds_read_b128 v[214:217], v146 offset:6720
	ds_read_b128 v[218:221], v146 offset:6736
	ds_read_b128 v[222:225], v146 offset:128
	ds_read_b128 v[226:229], v146 offset:144
	v_exp_f32_e32 v230, v74
	v_exp_f32_e32 v75, v75
	v_exp_f32_e32 v76, v76
	v_exp_f32_e32 v147, v69
	v_exp_f32_e32 v77, v77
	v_exp_f32_e32 v148, v70
	v_exp_f32_e32 v78, v78
	v_exp_f32_e32 v149, v71
	v_exp_f32_e32 v79, v79
	v_add_f32_e32 v69, v200, v204
	v_add_f32_e32 v70, v66, v67
	v_add_f32_e32 v71, v230, v75
	v_exp_f32_e32 v188, v72
	v_exp_f32_e32 v80, v80
	s_waitcnt lgkmcnt(6)
	v_mfma_f32_32x32x64_f8f6f4 v[82:97], v[138:145], v[130:137], v[238:253]
	ds_read_b128 v[138:141], v146 offset:6784
	ds_read_b128 v[142:145], v146 offset:6800
	v_exp_f32_e32 v146, v68
	v_add_f32_e32 v68, v198, v202
	v_add_f32_e32 v68, v190, v68
	v_add_f32_e32 v69, v194, v69
	v_add_f32_e32 v70, v146, v70
	v_add_f32_e32 v71, v76, v71
	v_exp_f32_e32 v189, v73
	v_exp_f32_e32 v81, v81
	v_add_f32_e32 v68, v191, v68
	v_add_f32_e32 v69, v195, v69
	v_add_f32_e32 v70, v147, v70
	v_add_f32_e32 v71, v77, v71
	v_add_f32_e32 v68, v199, v68
	v_add_f32_e32 v69, v201, v69
	s_waitcnt lgkmcnt(6)
	v_mfma_f32_32x32x64_f8f6f4 v[98:113], v[206:213], v[122:129], v[98:113]
	v_add_f32_e32 v70, v148, v70
	v_add_f32_e32 v71, v78, v71
	v_add_f32_e32 v68, v203, v68
	v_add_f32_e32 v69, v205, v69
	v_add_f32_e32 v70, v149, v70
	v_add_f32_e32 v71, v79, v71
	v_add_f32_e32 v68, v192, v68
	v_add_f32_e32 v69, v196, v69
	v_add_f32_e32 v70, v188, v70
	v_add_f32_e32 v71, v80, v71
	v_add_f32_e32 v68, v193, v68
	v_add_f32_e32 v69, v197, v69
	v_add_f32_e32 v70, v189, v70
	v_add_f32_e32 v71, v81, v71
	v_mov_b32_e32 v73, 0
	s_waitcnt lgkmcnt(4)
	v_mfma_f32_32x32x64_f8f6f4 v[82:97], v[214:221], v[122:129], v[82:97]
	v_add_f32_e32 v68, v69, v68
	v_add_f32_e32 v69, v71, v70
	v_cvt_pk_fp8_f32 v73, v148, v149
	v_mov_b32_e32 v74, 0
	v_add_f32_e32 v187, v68, v69
	v_mov_b32_e32 v68, 0
	v_mov_b32_e32 v69, 0
	v_mov_b32_e32 v70, 0
	v_mov_b32_e32 v71, 0
	v_mov_b32_e32 v72, 0
	v_cvt_pk_fp8_f32 v74, v230, v75
	v_mov_b32_e32 v75, 0
	v_cvt_pk_fp8_f32 v68, v198, v202
	v_cvt_pk_fp8_f32 v69, v199, v203
	v_cvt_pk_fp8_f32 v70, v200, v204
	s_waitcnt lgkmcnt(2)
	v_mfma_f32_32x32x64_f8f6f4 v[98:113], v[222:229], v[114:121], v[98:113]
	v_cvt_pk_fp8_f32 v71, v201, v205
	v_cvt_pk_fp8_f32 v72, v66, v67
	v_cvt_pk_fp8_f32 v75, v78, v79
	v_cvt_pk_fp8_f32 v73, v188, v189 op_sel:[0,0,1]
	v_mov_b32_e32 v188, v187
	s_nop 1
	v_permlane32_swap_b32_e32 v187, v188
	v_cvt_pk_fp8_f32 v68, v190, v191 op_sel:[0,0,1]
	v_cvt_pk_fp8_f32 v69, v192, v193 op_sel:[0,0,1]
	v_cvt_pk_fp8_f32 v70, v194, v195 op_sel:[0,0,1]
	v_cvt_pk_fp8_f32 v71, v196, v197 op_sel:[0,0,1]
	v_cvt_pk_fp8_f32 v72, v146, v147 op_sel:[0,0,1]
	v_cvt_pk_fp8_f32 v74, v76, v77 op_sel:[0,0,1]
	v_cvt_pk_fp8_f32 v75, v80, v81 op_sel:[0,0,1]
	s_waitcnt lgkmcnt(0)
	v_mfma_f32_32x32x64_f8f6f4 v[82:97], v[138:145], v[114:121], v[82:97]
	s_mul_i32 s51, s47, 0x2800
	v_add_u32_e32 v66, s51, v171
	ds_read_b128 v[138:141], v66
	ds_read_b128 v[142:145], v66 offset:16
	v_max_f32_e32 v67, v98, v98
	v_max_f32_e32 v76, v106, v106
	s_nop 13
	v_max_f32_e32 v77, v90, v90
	v_mov_b32_e32 v189, 1.0
	s_waitcnt lgkmcnt(0)
	v_mfma_f32_32x32x64_f8f6f4 v[2:17], v[68:75], v[138:145], v[2:17]
	ds_read_b128 v[138:141], v66 offset:2560
	ds_read_b128 v[142:145], v66 offset:2576
	ds_read_b128 v[190:193], v66 offset:5120
	ds_read_b128 v[194:197], v66 offset:5136
	ds_read_b128 v[198:201], v66 offset:7680
	ds_read_b128 v[202:205], v66 offset:7696
	v_max_f32_e32 v66, v99, v99
	v_max_f32_e32 v66, v67, v66
	v_max_f32_e32 v67, v107, v107
	v_max_f32_e32 v67, v76, v67
	v_max_f32_e32 v76, v91, v91
	v_max_f32_e32 v76, v77, v76
	v_max3_f32 v77, v82, v83, v84
	v_max3_f32 v76, v76, v92, v93
	v_max3_f32 v66, v66, v100, v101
	v_max3_f32 v67, v67, v108, v109
	v_max3_f32 v77, v77, v85, v86
	v_max3_f32 v76, v76, v94, v95
	v_max3_f32 v66, v66, v102, v103
	v_max3_f32 v67, v67, v110, v111
	s_waitcnt lgkmcnt(4)
	v_mfma_f32_32x32x64_f8f6f4 v[50:65], v[68:75], v[138:145], v[50:65]
	v_max3_f32 v77, v77, v87, v88
	v_max3_f32 v76, v76, v96, v97
	v_max3_f32 v66, v66, v104, v105
	v_max3_f32 v67, v67, v112, v113
	v_max3_f32 v76, v77, v89, v76
	v_max3_f32 v66, v66, v67, v76
	v_mov_b32_e32 v67, v66
	s_nop 1
	v_permlane32_swap_b32_e32 v66, v67
	v_max_f32_e32 v67, v67, v67
	v_max_f32_e32 v66, v66, v66
	v_max_f32_e32 v66, v66, v67
	v_cmp_ge_f32_e32 vcc, s43, v66
	s_cmp_eq_u64 vcc, exec
	s_waitcnt lgkmcnt(2)
	v_mfma_f32_32x32x64_f8f6f4 v[34:49], v[68:75], v[190:197], v[34:49]
	s_waitcnt lgkmcnt(0)
	v_mfma_f32_32x32x64_f8f6f4 v[18:33], v[68:75], v[198:205], v[18:33]
	s_cbranch_scc0 .LBB0_2170
	v_cmp_gt_f32_e32 vcc, 1.0, v189
	s_cbranch_vccz .LBB0_2163

; #define LAS __attribute__((address_space(3)))
; #define SBAR() __builtin_amdgcn_sched_barrier(0)
; #define SLOAD(k0) do { sv0 = *reinterpret_cast<const u32x4*>(Vh + (size_t)(k0) + vgo); \
;     const unsigned char* kp_ = Kh + (size_t)(k0) * LDKK; sk0 = *reinterpret_cast<const u32x4*>(kp_ + kgo0); sk1 = *reinterpret_cast<const u32x4*>(kp_ + kgo1); } while (0)
; #define SWRITE(b) do { *(u32x4*)(V_lds + (b) * SHM_V + vlo) = sv0; \
;     *(u32x4*)(K_lds + (b) * SHM_K + klo0) = sk0; *(u32x4*)(K_lds + (b) * SHM_K + klo1) = sk1; } while (0)
; #define SWAIT() asm volatile("s_waitcnt vmcnt(0)" ::: "memory")
; __device__ __forceinline__ void qkt(f32x16& p0, f32x16& p1, const int kb, const pg8::i32x8 (&qf)[3], float minit) {
; #pragma unroll
;     for (int r = 0; r < 16; ++r) { p0[r] = -minit; p1[r] = -minit; }
; #pragma unroll
;     for (int s = 0; s < 3; ++s) {
;         const u32x4 a0 = *reinterpret_cast<const LAS u32x4*>((uintptr_t)(unsigned)(kb + (s * 64))), a1 = *reinterpret_cast<const LAS u32x4*>((uintptr_t)(unsigned)(kb + (s * 64 + 16)));
;         const u32x4 b0 = *reinterpret_cast<const LAS u32x4*>((uintptr_t)(unsigned)(kb + (s * 64 + 32 * KROW))), b1 = *reinterpret_cast<const LAS u32x4*>((uintptr_t)(unsigned)(kb + (s * 64 + 32 * KROW + 16)));
;         const pg8::i32x8 A0 = {(int)a0.x, (int)a0.y, (int)a0.z, (int)a0.w, (int)a1.x, (int)a1.y, (int)a1.z, (int)a1.w}, A1 = {(int)b0.x, (int)b0.y, (int)b0.z, (int)b0.w, (int)b1.x, (int)b1.y, (int)b1.z, (int)b1.w};
;         p0 = __builtin_amdgcn_mfma_scale_f32_32x32x64_f8f6f4(A0, qf[s], p0, 0, 0, 0, 0, 0, 0);
;         p1 = __builtin_amdgcn_mfma_scale_f32_32x32x64_f8f6f4(A1, qf[s], p1, 0, 0, 0, 0, 0, 0);
;     }
; }
; __device__ __forceinline__ void attn_body(const unsigned char* __restrict__ Qb, const unsigned char* __restrict__ Kh, const unsigned char* __restrict__ Vh, bf16_t* __restrict__ Ob, int seq, char* lds) {
;     ...
;         SWAIT(); SWRITE(bm); SLOAD(min((j + 3) * KVBLK, klast)); SBAR();
;         qkt(pA0, pA1, kb + bn * SHM_K, qf, m_reg);
;         finishSM(pB0, pB1, alB, l_reg, pa); SBAR();
;         pv_d0(o, vb0 + bc * SHM_V, pa); partialSM_shift(pA0, pA1, m_reg, alA);
;         RESC(alA); __syncthreads();
.LBB0_2163:
	s_mul_i32 s6, s47, 0x3400
	s_add_i32 s52, s6, 0
	s_add_i32 s6, s16, 0xc693ff80
	s_min_u32 s6, s6, 0x1000
	s_mul_i32 s18, s6, 0x600
	s_add_i32 s18, s18, 0x48000
	s_add_u32 s18, s14, s18
	s_barrier
	s_waitcnt vmcnt(0)
	v_lshl_add_u64 v[66:67], v[172:173], 0, s[6:7]
	s_addc_u32 s19, s15, 0
	v_lshl_add_u64 v[68:69], s[18:19], 0, v[162:163]
	global_load_dwordx4 v[146:149], v[66:67], off offset:192
	global_load_dwordx4 v[138:141], v[68:69], off
	v_lshl_add_u64 v[66:67], s[18:19], 0, v[166:167]
	global_load_dwordx4 v[142:145], v[66:67], off
	v_add_u32_e32 v66, s51, v184
	s_waitcnt vmcnt(5)
	ds_write_b128 v66, v[158:161]
	v_add_u32_e32 v66, s52, v168
	s_waitcnt vmcnt(4)
	ds_write_b128 v66, v[154:157] offset:30720
	v_add_u32_e32 v66, s52, v170
	v_exp_f32_e32 v222, v98
	v_exp_f32_e32 v223, v99
	v_exp_f32_e32 v224, v100
	v_exp_f32_e32 v225, v101
	v_exp_f32_e32 v226, v102
	v_exp_f32_e32 v227, v103
	v_exp_f32_e32 v228, v104
	v_exp_f32_e32 v229, v105
	v_exp_f32_e32 v230, v106
	v_exp_f32_e32 v231, v107
	v_exp_f32_e32 v232, v108
	v_exp_f32_e32 v233, v109
	v_exp_f32_e32 v234, v110
	v_exp_f32_e32 v235, v111
	v_exp_f32_e32 v236, v112
	v_exp_f32_e32 v237, v113
	s_waitcnt vmcnt(3)
	ds_write_b128 v66, v[150:153] offset:30720
	v_add_u32_e32 v158, s50, v183
	ds_read_b128 v[150:153], v158
	ds_read_b128 v[154:157], v158 offset:16
	v_exp_f32_e32 v83, v83
	v_exp_f32_e32 v84, v84
	s_waitcnt lgkmcnt(0)
	v_mfma_f32_32x32x64_f8f6f4 v[98:113], v[150:157], v[130:137], v[238:253]
	ds_read_b128 v[150:153], v158 offset:6656
	ds_read_b128 v[154:157], v158 offset:6672
	ds_read_b128 v[190:193], v158 offset:64
	ds_read_b128 v[194:197], v158 offset:80
	ds_read_b128 v[198:201], v158 offset:6720
	ds_read_b128 v[202:205], v158 offset:6736
	ds_read_b128 v[206:209], v158 offset:128
	ds_read_b128 v[210:213], v158 offset:144
	ds_read_b128 v[214:217], v158 offset:6784
	ds_read_b128 v[218:221], v158 offset:6800
	v_exp_f32_e32 v85, v85
	v_exp_f32_e32 v158, v93
	v_exp_f32_e32 v94, v94
	v_exp_f32_e32 v95, v95
	v_exp_f32_e32 v96, v96
	v_exp_f32_e32 v97, v97
	v_mov_b32_e32 v93, 0
	v_cvt_pk_fp8_f32 v93, v94, v95
	v_cvt_pk_fp8_f32 v93, v96, v97 op_sel:[0,0,1]
	s_waitcnt lgkmcnt(8)
	v_mfma_f32_32x32x64_f8f6f4 v[66:81], v[150:157], v[130:137], v[238:253]
	v_exp_f32_e32 v150, v82
	v_exp_f32_e32 v155, v90
	v_exp_f32_e32 v156, v91
	v_exp_f32_e32 v157, v92
	v_exp_f32_e32 v151, v86
	v_exp_f32_e32 v152, v87
	v_exp_f32_e32 v153, v88
	v_add_f32_e32 v82, v223, v222
	v_add_f32_e32 v86, v231, v230
	v_add_f32_e32 v87, v150, v83
	v_add_f32_e32 v88, v155, v156
	v_add_f32_e32 v82, v224, v82
	v_add_f32_e32 v86, v232, v86
	v_add_f32_e32 v87, v84, v87
	v_add_f32_e32 v88, v157, v88
	s_waitcnt lgkmcnt(6)
	v_mfma_f32_32x32x64_f8f6f4 v[98:113], v[190:197], v[122:129], v[98:113]
	v_exp_f32_e32 v154, v89
	v_add_f32_e32 v82, v225, v82
	v_add_f32_e32 v86, v233, v86
	v_add_f32_e32 v87, v85, v87
	v_add_f32_e32 v88, v158, v88
	v_add_f32_e32 v82, v226, v82
	v_add_f32_e32 v86, v234, v86
	v_add_f32_e32 v87, v151, v87
	v_add_f32_e32 v88, v94, v88
	v_add_f32_e32 v82, v227, v82
	v_add_f32_e32 v86, v235, v86
	v_add_f32_e32 v87, v152, v87
	v_add_f32_e32 v88, v95, v88
	v_add_f32_e32 v82, v228, v82
	v_add_f32_e32 v86, v236, v86
	s_waitcnt lgkmcnt(4)
	v_mfma_f32_32x32x64_f8f6f4 v[66:81], v[198:205], v[122:129], v[66:81]
	v_add_f32_e32 v87, v153, v87
	v_add_f32_e32 v88, v96, v88
	v_add_f32_e32 v82, v229, v82
	v_add_f32_e32 v86, v237, v86
	v_add_f32_e32 v87, v154, v87
	v_add_f32_e32 v88, v97, v88
	v_add_f32_e32 v82, v86, v82
	v_add_f32_e32 v86, v88, v87
	v_add_f32_e32 v82, v82, v86
	v_mov_b32_e32 v86, 0
	v_mov_b32_e32 v87, 0
	v_mov_b32_e32 v88, 0
	v_mov_b32_e32 v89, 0
	v_mov_b32_e32 v90, 0
	v_mov_b32_e32 v91, 0
	s_waitcnt lgkmcnt(2)
	v_mfma_f32_32x32x64_f8f6f4 v[98:113], v[206:213], v[114:121], v[98:113]
	v_mov_b32_e32 v92, 0
	v_cvt_pk_fp8_f32 v86, v222, v223
	v_cvt_pk_fp8_f32 v87, v226, v227
	v_cvt_pk_fp8_f32 v88, v230, v231
	v_cvt_pk_fp8_f32 v89, v234, v235
	v_cvt_pk_fp8_f32 v90, v150, v83
	v_cvt_pk_fp8_f32 v91, v151, v152
	v_cvt_pk_fp8_f32 v92, v155, v156
	v_mov_b32_e32 v83, v82
	s_nop 1
	v_permlane32_swap_b32_e32 v82, v83
	v_cvt_pk_fp8_f32 v86, v224, v225 op_sel:[0,0,1]
	v_cvt_pk_fp8_f32 v87, v228, v229 op_sel:[0,0,1]
	v_cvt_pk_fp8_f32 v88, v232, v233 op_sel:[0,0,1]
	v_cvt_pk_fp8_f32 v89, v236, v237 op_sel:[0,0,1]
	s_waitcnt lgkmcnt(0)
	v_mfma_f32_32x32x64_f8f6f4 v[66:81], v[214:221], v[114:121], v[66:81]
	v_cvt_pk_fp8_f32 v90, v84, v85 op_sel:[0,0,1]
	v_cvt_pk_fp8_f32 v91, v153, v154 op_sel:[0,0,1]
	v_cvt_pk_fp8_f32 v92, v157, v158 op_sel:[0,0,1]
	s_mul_i32 s6, s49, 0x2800
	v_add_u32_e32 v84, s6, v171
	ds_read_b128 v[150:153], v84
	ds_read_b128 v[154:157], v84 offset:16
	v_max_f32_e32 v85, v98, v98
	v_max_f32_e32 v94, v106, v106
	s_nop 10
	v_max_f32_e32 v95, v74, v74
	s_waitcnt lgkmcnt(0)
	v_mfma_f32_32x32x64_f8f6f4 v[2:17], v[86:93], v[150:157], v[2:17]
	ds_read_b128 v[150:153], v84 offset:2560
	ds_read_b128 v[154:157], v84 offset:2576
	ds_read_b128 v[190:193], v84 offset:5120
	ds_read_b128 v[194:197], v84 offset:5136
	ds_read_b128 v[198:201], v84 offset:7680
	ds_read_b128 v[202:205], v84 offset:7696
	v_max_f32_e32 v84, v99, v99
	v_max_f32_e32 v84, v85, v84
	v_max_f32_e32 v85, v107, v107
	v_max_f32_e32 v85, v94, v85
	v_max_f32_e32 v94, v75, v75
	v_max_f32_e32 v94, v95, v94
	v_max3_f32 v95, v66, v67, v68
	v_max3_f32 v94, v94, v76, v77
	v_max3_f32 v84, v84, v100, v101
	v_max3_f32 v85, v85, v108, v109
	v_max3_f32 v95, v95, v69, v70
	v_max3_f32 v94, v94, v78, v79
	v_max3_f32 v84, v84, v102, v103
	v_max3_f32 v85, v85, v110, v111
	s_waitcnt lgkmcnt(4)
	v_mfma_f32_32x32x64_f8f6f4 v[50:65], v[86:93], v[150:157], v[50:65]
	v_max3_f32 v95, v95, v71, v72
	v_max3_f32 v94, v94, v80, v81
	v_max3_f32 v84, v84, v104, v105
	v_max3_f32 v85, v85, v112, v113
	v_max3_f32 v94, v95, v73, v94
	v_max3_f32 v84, v84, v85, v94
	v_mov_b32_e32 v85, v84
	s_nop 1
	v_permlane32_swap_b32_e32 v84, v85
	v_max_f32_e32 v85, v85, v85
	v_max_f32_e32 v84, v84, v84
	v_max_f32_e32 v84, v84, v85
	v_cmp_ge_f32_e32 vcc, s43, v84
	s_cmp_eq_u64 vcc, exec
	v_mov_b32_e32 v150, 1.0
	s_waitcnt lgkmcnt(2)
	v_mfma_f32_32x32x64_f8f6f4 v[34:49], v[86:93], v[190:197], v[34:49]
	s_waitcnt lgkmcnt(0)
	v_mfma_f32_32x32x64_f8f6f4 v[18:33], v[86:93], v[198:205], v[18:33]
	s_cbranch_scc0 .LBB0_2171
	v_cmp_gt_f32_e32 vcc, 1.0, v150
	s_cbranch_vccz .LBB0_2168

; __device__ __forceinline__ void partialSM_shift(f32x16& p0, f32x16& p1, float& m_reg, float& alpha) {
;     ...
;     else { const float d = fmaxf(pmax, 0.f); alpha = __builtin_amdgcn_exp2f(-d); m_reg += d;
; #pragma unroll
;         for (int r = 0; r < 16; ++r) p0[r] = p0[r] - d;
; #pragma unroll
;         for (int r = 0; r < 16; ++r) p1[r] = p1[r] - d; }
; __device__ __forceinline__ void qkt(f32x16& p0, f32x16& p1, const int kb, const pg8::i32x8 (&qf)[3], float minit) {
; #pragma unroll
;     for (int r = 0; r < 16; ++r) { p0[r] = -minit; p1[r] = -minit; }
.LBB0_2170:
	v_max_f32_e32 v66, v66, v66
	v_max_f32_e32 v66, 0, v66
	v_exp_f32_e64 v189, -v66
	v_add_f32_e32 v185, v185, v66
	v_xor_b32_e32 v238, 0x80000000, v185
	v_mov_b32_e32 v239, v238
	v_mov_b32_e32 v240, v238
	v_mov_b32_e32 v241, v238
	v_mov_b32_e32 v242, v238
	v_mov_b32_e32 v243, v238
	v_mov_b32_e32 v244, v238
	v_mov_b32_e32 v245, v238
	v_mov_b32_e32 v246, v238
	v_mov_b32_e32 v247, v238
	v_mov_b32_e32 v248, v238
	v_mov_b32_e32 v249, v238
	v_mov_b32_e32 v250, v238
	v_mov_b32_e32 v251, v238
	v_mov_b32_e32 v252, v238
	v_mov_b32_e32 v253, v238
	v_pk_add_f32 v[98:99], v[98:99], v[66:67] op_sel_hi:[1,0] neg_lo:[0,1] neg_hi:[0,1]
	v_pk_add_f32 v[100:101], v[100:101], v[66:67] op_sel_hi:[1,0] neg_lo:[0,1] neg_hi:[0,1]
	v_pk_add_f32 v[102:103], v[102:103], v[66:67] op_sel_hi:[1,0] neg_lo:[0,1] neg_hi:[0,1]
	v_pk_add_f32 v[104:105], v[104:105], v[66:67] op_sel_hi:[1,0] neg_lo:[0,1] neg_hi:[0,1]
	v_pk_add_f32 v[106:107], v[106:107], v[66:67] op_sel_hi:[1,0] neg_lo:[0,1] neg_hi:[0,1]
	v_pk_add_f32 v[108:109], v[108:109], v[66:67] op_sel_hi:[1,0] neg_lo:[0,1] neg_hi:[0,1]
	v_pk_add_f32 v[110:111], v[110:111], v[66:67] op_sel_hi:[1,0] neg_lo:[0,1] neg_hi:[0,1]
	v_pk_add_f32 v[112:113], v[112:113], v[66:67] op_sel_hi:[1,0] neg_lo:[0,1] neg_hi:[0,1]
	v_sub_f32_e32 v97, v97, v66
	v_sub_f32_e32 v96, v96, v66
	v_sub_f32_e32 v95, v95, v66
	v_sub_f32_e32 v94, v94, v66
	v_sub_f32_e32 v93, v93, v66
	v_sub_f32_e32 v92, v92, v66
	v_sub_f32_e32 v91, v91, v66
	v_sub_f32_e32 v90, v90, v66
	v_sub_f32_e32 v89, v89, v66
	v_sub_f32_e32 v88, v88, v66
	v_sub_f32_e32 v87, v87, v66
	v_sub_f32_e32 v86, v86, v66
	v_sub_f32_e32 v85, v85, v66
	v_sub_f32_e32 v84, v84, v66
	v_sub_f32_e32 v83, v83, v66
	v_sub_f32_e32 v82, v82, v66
	v_cmp_gt_f32_e32 vcc, 1.0, v189
	s_cbranch_vccnz .LBB0_2160
	s_branch .LBB0_2163
.LBB0_2171:
	v_max_f32_e32 v84, v84, v84
	v_max_f32_e32 v84, 0, v84
	v_exp_f32_e64 v150, -v84
	v_add_f32_e32 v185, v185, v84
	v_xor_b32_e32 v238, 0x80000000, v185
	v_mov_b32_e32 v239, v238
	v_mov_b32_e32 v240, v238
	v_mov_b32_e32 v241, v238
	v_mov_b32_e32 v242, v238
	v_mov_b32_e32 v243, v238
	v_mov_b32_e32 v244, v238
	v_mov_b32_e32 v245, v238
	v_mov_b32_e32 v246, v238
	v_mov_b32_e32 v247, v238
	v_mov_b32_e32 v248, v238
	v_mov_b32_e32 v249, v238
	v_mov_b32_e32 v250, v238
	v_mov_b32_e32 v251, v238
	v_mov_b32_e32 v252, v238
	v_mov_b32_e32 v253, v238
	v_pk_add_f32 v[98:99], v[98:99], v[84:85] op_sel_hi:[1,0] neg_lo:[0,1] neg_hi:[0,1]
	v_pk_add_f32 v[100:101], v[100:101], v[84:85] op_sel_hi:[1,0] neg_lo:[0,1] neg_hi:[0,1]
	v_pk_add_f32 v[102:103], v[102:103], v[84:85] op_sel_hi:[1,0] neg_lo:[0,1] neg_hi:[0,1]
	v_pk_add_f32 v[104:105], v[104:105], v[84:85] op_sel_hi:[1,0] neg_lo:[0,1] neg_hi:[0,1]
	v_pk_add_f32 v[106:107], v[106:107], v[84:85] op_sel_hi:[1,0] neg_lo:[0,1] neg_hi:[0,1]
	v_pk_add_f32 v[108:109], v[108:109], v[84:85] op_sel_hi:[1,0] neg_lo:[0,1] neg_hi:[0,1]
	v_pk_add_f32 v[110:111], v[110:111], v[84:85] op_sel_hi:[1,0] neg_lo:[0,1] neg_hi:[0,1]
	v_pk_add_f32 v[112:113], v[112:113], v[84:85] op_sel_hi:[1,0] neg_lo:[0,1] neg_hi:[0,1]
	v_sub_f32_e32 v81, v81, v84
	v_sub_f32_e32 v80, v80, v84
	v_sub_f32_e32 v79, v79, v84
	v_sub_f32_e32 v78, v78, v84
	v_sub_f32_e32 v77, v77, v84
	v_sub_f32_e32 v76, v76, v84
	v_sub_f32_e32 v75, v75, v84
	v_sub_f32_e32 v74, v74, v84
	v_sub_f32_e32 v73, v73, v84
	v_sub_f32_e32 v72, v72, v84
	v_sub_f32_e32 v71, v71, v84
	v_sub_f32_e32 v70, v70, v84
	v_sub_f32_e32 v69, v69, v84
	v_sub_f32_e32 v68, v68, v84
	v_sub_f32_e32 v67, v67, v84
	v_sub_f32_e32 v66, v66, v84
	v_cmp_gt_f32_e32 vcc, 1.0, v150
	s_cbranch_vccnz .LBB0_2165
	s_branch .LBB0_2168

; __global__ void __launch_bounds__(512, 2) fwd_kernel(Params KP) {
	.amdhsa_kernel _Z10fwd_kernel6Params
		.amdhsa_group_segment_fixed_size 0
		.amdhsa_private_segment_fixed_size 0
		.amdhsa_kernarg_size 312
		.amdhsa_user_sgpr_count 2
		.amdhsa_user_sgpr_dispatch_ptr 0
		.amdhsa_user_sgpr_queue_ptr 0
		.amdhsa_user_sgpr_kernarg_segment_ptr 1
		.amdhsa_user_sgpr_dispatch_id 0
		.amdhsa_user_sgpr_kernarg_preload_length 0
		.amdhsa_user_sgpr_kernarg_preload_offset 0
		.amdhsa_user_sgpr_private_segment_size 0
		.amdhsa_uses_dynamic_stack 0
		.amdhsa_enable_private_segment 0
		.amdhsa_system_sgpr_workgroup_id_x 1
		.amdhsa_system_sgpr_workgroup_id_y 0
		.amdhsa_system_sgpr_workgroup_id_z 0
		.amdhsa_system_sgpr_workgroup_info 0
		.amdhsa_system_vgpr_workitem_id 0
		.amdhsa_next_free_vgpr 256
		.amdhsa_next_free_sgpr 102
		.amdhsa_accum_offset 256
		.amdhsa_reserve_vcc 1
		.amdhsa_float_round_mode_32 0
		.amdhsa_float_round_mode_16_64 0
		.amdhsa_float_denorm_mode_32 3
		.amdhsa_float_denorm_mode_16_64 3
		.amdhsa_dx10_clamp 1
		.amdhsa_ieee_mode 1
		.amdhsa_fp16_overflow 0
		.amdhsa_tg_split 0
		.amdhsa_exception_fp_ieee_invalid_op 0
		.amdhsa_exception_fp_denorm_src 0
		.amdhsa_exception_fp_ieee_div_zero 0
		.amdhsa_exception_fp_ieee_overflow 0
		.amdhsa_exception_fp_ieee_underflow 0
		.amdhsa_exception_fp_ieee_inexact 0
		.amdhsa_exception_int_div_zero 0
	.end_amdhsa_kernel

; __global__ void __launch_bounds__(512, 2) fwd_kernel(Params KP) {
amdhsa.kernels:
  - .agpr_count:     0
    .args:
      - .offset:         0
        .size:           312
        .value_kind:     by_value
    .group_segment_fixed_size: 0
    .kernarg_segment_align: 8
    .kernarg_segment_size: 312
    .language:       OpenCL C
    .language_version:
      - 2
      - 0
    .max_flat_workgroup_size: 512
    .name:           _Z10fwd_kernel6Params
    .private_segment_fixed_size: 0
    .sgpr_count:     108
    .sgpr_spill_count: 0
    .symbol:         _Z10fwd_kernel6Params.kd
    .uniform_work_group_size: 1
    .uses_dynamic_stack: false
    .vgpr_count:     256
    .vgpr_spill_count: 0
    .wavefront_size: 64
